# attention phase: each workgroup touches the query rows of all its units at the start of the phase (L2 warm-up), on top of the combine-phase changes
# baseline (speedup 1.0000x reference)
.LBB0_420:
	v_readlane_b32 s0, v255, 8
	s_and_b32 s1, s0, 31
	s_lshl_b32 s1, s1, 8
	s_lshr_b32 s6, s0, 7
	s_lshl_b32 s6, s6, 13
	s_add_u32 s1, s1, s6
	v_readfirstlane_b32 s6, v0
	s_lshr_b32 s6, s6, 6
	s_lshl_b32 s6, s6, 5
	s_add_u32 s1, s1, s6
	s_mul_i32 s1, s1, 0xf00
	s_bfe_u32 s6, s0, 0x20005
	v_readlane_b32 s10, v255, 31
	v_readlane_b32 s11, v255, 32
	s_add_u32 s10, s10, s1
	s_addc_u32 s11, s11, 0
	v_lshrrev_b32_e32 v187, 1, v1
	v_mul_u32_u24_e32 v187, 0xf00, v187
	v_and_b32_e32 v188, 1, v1
	v_lshl_add_u32 v187, v188, 7, v187
	s_lshl_b32 s7, s6, 8
	v_add_u32_e32 v189, s7, v187
	global_load_dword v190, v189, s[10:11]
	v_lshrrev_b32_e32 v187, 1, v1
	v_mul_u32_u24_e32 v187, 0xf00, v187
	v_lshl_add_u32 v187, v188, 8, v187
	s_lshl_b32 s7, s6, 6
	s_addk_i32 s7, 0x600
	v_add_u32_e32 v189, s7, v187
	global_load_dword v190, v189, s[10:11]
	v_and_b32_e32 v187, 31, v1
	v_mul_u32_u24_e32 v187, 0xf00, v187
	s_addk_i32 s7, 0x200
	v_add_u32_e32 v189, s7, v187
	global_load_dword v190, v189, s[10:11]
	s_mov_b64 s[0:1], 0
	s_waitcnt vmcnt(0)
	v_mov_b32_e32 v4, v161
	v_mov_b32_e32 v5, v0
	s_branch .LBB0_422
